# v13 + one static s_setprio 1 for waves 0-3 (the other half) before the attention queues
# speedup vs baseline: 1.0055x; 1.0017x over previous
.LBB0_6667:
	global_load_dword v11, v[4:5], off
	v_max_f32_e32 v10, v10, v10
	v_add_co_u32_e32 v1, vcc, 64, v1
	s_xor_b64 s[2:3], vcc, -1
	v_max_f32_e32 v2, v2, v2
	s_and_b64 s[2:3], exec, s[2:3]
	v_lshl_add_u64 v[4:5], v[4:5], 0, s[4:5]
	s_or_b64 s[0:1], s[2:3], s[0:1]
	s_waitcnt vmcnt(0)
	v_max_f32_e64 v11, |v11|, |v11|
	v_max_f32_e32 v10, v10, v11
	global_load_dword v11, v[6:7], off
	v_lshl_add_u64 v[6:7], v[6:7], 0, s[4:5]
	s_waitcnt vmcnt(0)
	v_max_f32_e64 v11, |v11|, |v11|
	v_max_f32_e32 v2, v2, v11
	s_andn2_b64 exec, exec, s[0:1]
	s_cbranch_execnz .LBB0_6667
	s_or_b64 exec, exec, s[0:1]
	v_and_b32_e32 v1, 64, v224
	v_add_u32_e32 v4, 64, v1
	v_xor_b32_e32 v1, 32, v224
	v_cmp_lt_i32_e32 vcc, v1, v4
	v_max_f32_e32 v6, v9, v9
	v_max_f32_e32 v7, v8, v8
	v_cndmask_b32_e32 v1, v224, v1, vcc
	v_lshlrev_b32_e32 v1, 2, v1
	ds_bpermute_b32 v5, v1, v9
	s_mov_b32 s0, 0x42c00000
	v_cmp_eq_u32_e64 s[38:39], 0, v197
	s_waitcnt lgkmcnt(0)
	v_max_f32_e32 v5, v5, v5
	v_max_f32_e32 v5, v6, v5
	ds_bpermute_b32 v6, v1, v8
	v_max_f32_e32 v8, v10, v10
	s_waitcnt lgkmcnt(0)
	v_max_f32_e32 v6, v6, v6
	v_max_f32_e32 v6, v7, v6
	ds_bpermute_b32 v7, v1, v10
	ds_bpermute_b32 v1, v1, v2
	v_max_f32_e32 v2, v2, v2
	s_waitcnt lgkmcnt(1)
	v_max_f32_e32 v7, v7, v7
	s_waitcnt lgkmcnt(0)
	v_max_f32_e32 v1, v1, v1
	v_max_f32_e32 v1, v2, v1
	v_xor_b32_e32 v2, 16, v224
	v_cmp_lt_i32_e32 vcc, v2, v4
	v_max_f32_e32 v7, v8, v7
	s_nop 0
	v_cndmask_b32_e32 v2, v224, v2, vcc
	v_lshlrev_b32_e32 v2, 2, v2
	ds_bpermute_b32 v8, v2, v5
	s_waitcnt lgkmcnt(0)
	v_max_f32_e32 v8, v8, v8
	v_max_f32_e32 v5, v5, v8
	ds_bpermute_b32 v8, v2, v6
	s_waitcnt lgkmcnt(0)
	v_max_f32_e32 v8, v8, v8
	v_max_f32_e32 v6, v6, v8
	ds_bpermute_b32 v8, v2, v7
	ds_bpermute_b32 v2, v2, v1
	s_waitcnt lgkmcnt(1)
	v_max_f32_e32 v8, v8, v8
	s_waitcnt lgkmcnt(0)
	v_max_f32_e32 v2, v2, v2
	v_max_f32_e32 v1, v1, v2
	v_xor_b32_e32 v2, 8, v224
	v_cmp_lt_i32_e32 vcc, v2, v4
	v_max_f32_e32 v7, v7, v8
	s_nop 0
	v_cndmask_b32_e32 v2, v224, v2, vcc
	v_lshlrev_b32_e32 v193, 2, v2
	ds_bpermute_b32 v2, v193, v5
	s_waitcnt lgkmcnt(0)
	v_max_f32_e32 v2, v2, v2
	v_max_f32_e32 v2, v5, v2
	ds_bpermute_b32 v5, v193, v6
	s_waitcnt lgkmcnt(0)
	v_max_f32_e32 v5, v5, v5
	v_max_f32_e32 v5, v6, v5
	ds_bpermute_b32 v6, v193, v7
	s_waitcnt lgkmcnt(0)
	v_max_f32_e32 v6, v6, v6
	v_max_f32_e32 v6, v7, v6
	ds_bpermute_b32 v7, v193, v1
	s_waitcnt lgkmcnt(0)
	v_max_f32_e32 v7, v7, v7
	v_max_f32_e32 v1, v1, v7
	v_xor_b32_e32 v7, 4, v224
	v_cmp_lt_i32_e32 vcc, v7, v4
	s_nop 1
	v_cndmask_b32_e32 v7, v224, v7, vcc
	v_lshlrev_b32_e32 v194, 2, v7
	ds_bpermute_b32 v7, v194, v2
	s_waitcnt lgkmcnt(0)
	v_max_f32_e32 v7, v7, v7
	v_max_f32_e32 v2, v2, v7
	ds_bpermute_b32 v7, v194, v5
	s_waitcnt lgkmcnt(0)
	v_max_f32_e32 v7, v7, v7
	v_max_f32_e32 v5, v5, v7
	ds_bpermute_b32 v7, v194, v6
	s_waitcnt lgkmcnt(0)
	v_max_f32_e32 v7, v7, v7
	v_max_f32_e32 v6, v6, v7
	ds_bpermute_b32 v7, v194, v1
	s_waitcnt lgkmcnt(0)
	v_max_f32_e32 v7, v7, v7
	v_max_f32_e32 v7, v1, v7
	v_xor_b32_e32 v1, 2, v224
	v_cmp_lt_i32_e32 vcc, v1, v4
	s_nop 1
	v_cndmask_b32_e32 v1, v224, v1, vcc
	v_lshlrev_b32_e32 v195, 2, v1
	ds_bpermute_b32 v1, v195, v2
	s_waitcnt lgkmcnt(0)
	v_max_f32_e32 v1, v1, v1
	v_max_f32_e32 v2, v2, v1
	ds_bpermute_b32 v1, v195, v5
	s_waitcnt lgkmcnt(0)
	v_max_f32_e32 v1, v1, v1
	v_max_f32_e32 v5, v5, v1
	ds_bpermute_b32 v1, v195, v6
	s_waitcnt lgkmcnt(0)
	v_max_f32_e32 v1, v1, v1
	v_max_f32_e32 v1, v6, v1
	ds_bpermute_b32 v6, v195, v7
	s_waitcnt lgkmcnt(0)
	v_max_f32_e32 v6, v6, v6
	v_max_f32_e32 v199, v7, v6
	v_xor_b32_e32 v6, 1, v224
	v_cmp_lt_i32_e32 vcc, v6, v4
	s_nop 1
	v_cndmask_b32_e32 v4, v224, v6, vcc
	v_lshlrev_b32_e32 v196, 2, v4
	ds_bpermute_b32 v4, v196, v2
	ds_bpermute_b32 v201, v196, v1
	ds_bpermute_b32 v200, v196, v199
	s_waitcnt lgkmcnt(2)
	v_max_f32_e32 v4, v4, v4
	v_max_f32_e32 v2, v2, v4
	ds_bpermute_b32 v4, v196, v5
	v_mul_f32_e32 v2, 0x419fecaf, v2
	s_waitcnt lgkmcnt(0)
	v_max_f32_e32 v4, v4, v4
	v_max_f32_e32 v4, v5, v4
	v_mul_f32_e32 v2, v4, v2
	v_cmp_ngt_f32_e32 vcc, s0, v2
	s_nop 1
	v_cndmask_b32_e64 v2, 0, 1, vcc
	s_nop 0
	v_readfirstlane_b32 s0, v2
	s_bitcmp1_b32 s0, 0
	s_cselect_b64 s[0:1], -1, 0
	s_xor_b64 s[44:45], s[0:1], -1
	v_readfirstlane_b32 s2, v0
	s_nop 3
	s_lshr_b32 s2, s2, 6
	s_cmp_ge_u32 s2, 4
	s_cbranch_scc1 .Lattn_prio_done
	s_setprio 1
